# v22: v21 + attention O epilogue: in-quad 4x4 transpose on DPP, 8-byte row stores from every lane (16 stores per wave instead of 64 masked 4-byte ones), no bpermute round trips
# baseline (speedup 1.0000x reference)
; __device__ __forceinline__ int crow(int r, int hi) { return (r & 3) + 8 * (r >> 2) + 4 * hi; }
; template <class TIn, class TOut, int QS, int KS, int OS, bool BIAS, bool PREF = true>
; __device__ __forceinline__ void causal_swa_block(const BlockRef<TIn, TOut>& cur, const BlockRef<TIn, TOut>& nxt, int skv, int W, char* lds, Seam<TIn>& S) {
;     ...
;     if (hi == 0) li_l[r32] = l_reg; asm volatile("s_waitcnt lgkmcnt(0)" ::: "memory");
;     float rli[16];
; #pragma unroll
;     for (int r = 0; r < 16; ++r) rli[r] = __builtin_amdgcn_rcpf(li_l[crow(r, hi)]);
;     TOut* Ow = cur.O + (size_t)(wid * QBLK) * OS;
; #pragma unroll
;     for (int r = 0; r < 16; ++r) { const int orow = crow(r, hi);
; #pragma unroll
;         for (int d0 = 0; d0 < 4; ++d0) { const float v = o[d0][r] * rli[r];
;             if constexpr (same_t<TOut, float>::v) { Ow[(size_t)orow * OS + d0 * 32 + r32] = v; }
;             else { const float vn = __shfl_xor(v, 1);
;                    if ((r32 & 1) == 0) *(unsigned*)(Ow + (size_t)orow * OS + d0 * 32 + r32) = cvtpk(v, vn); } } }
.LBB0_503:
	s_waitcnt vmcnt(8)
	s_mov_b32 s15, 0
	s_waitcnt vmcnt(10)
	ds_write_b128 v215, v[102:105] offset:32768
	s_waitcnt vmcnt(8)
	ds_write_b128 v215, v[106:109] offset:40960
	v_cmp_gt_u32_e64 s[4:5], 32, v198
	s_and_saveexec_b64 s[0:1], s[4:5]
	ds_write_b32 v220, v114
	s_or_b64 exec, exec, s[0:1]
	s_waitcnt lgkmcnt(0)
	ds_read_b128 v[78:81], v219
	ds_read_b128 v[74:77], v219 offset:32
	s_add_u32 s29, s72, 0x17800000
	s_addc_u32 s28, s73, 0
	s_lshl_b64 s[0:1], s[16:17], 12
	s_waitcnt lgkmcnt(1)
	s_add_u32 s0, s29, s0
	s_addc_u32 s1, s28, s1
	s_add_u32 s2, s0, s10
	s_addc_u32 s3, s1, s11
	ds_read_b128 v[70:73], v219 offset:64
	ds_read_b128 v[66:69], v219 offset:96
	s_lshl_b64 s[0:1], s[14:15], 12
	s_add_u32 s0, s2, s0
	s_addc_u32 s1, s3, s1
	v_and_b32_e32 v82, 1, v0
	v_mov_b32_e32 v201, 0
	v_lshlrev_b32_e32 v200, 1, v216
	v_cmp_eq_u32_e64 s[2:3], 0, v82
	v_lshl_add_u64 v[82:83], s[0:1], 0, v[200:201]
	v_lshlrev_b32_e32 v202, 14, v218
	v_mov_b32_e32 v203, v201
	v_lshl_add_u64 v[82:83], v[82:83], 0, v[202:203]
	s_waitcnt lgkmcnt(0)
	v_rcp_f32_e32 v78, v78
	v_rcp_f32_e32 v79, v79
	v_rcp_f32_e32 v80, v80
	v_rcp_f32_e32 v81, v81
	v_rcp_f32_e32 v74, v74
	v_rcp_f32_e32 v75, v75
	v_rcp_f32_e32 v76, v76
	v_rcp_f32_e32 v77, v77
	v_rcp_f32_e32 v70, v70
	v_rcp_f32_e32 v71, v71
	v_rcp_f32_e32 v72, v72
	v_rcp_f32_e32 v73, v73
	v_rcp_f32_e32 v66, v66
	v_rcp_f32_e32 v67, v67
	v_rcp_f32_e32 v68, v68
	v_rcp_f32_e32 v69, v69
	v_mul_f32_e32 v50, v50, v78
	v_mul_f32_e32 v34, v34, v78
	v_mul_f32_e32 v18, v18, v78
	v_mul_f32_e32 v2, v2, v78
	v_mul_f32_e32 v51, v51, v79
	v_mul_f32_e32 v35, v35, v79
	v_mul_f32_e32 v19, v19, v79
	v_mul_f32_e32 v3, v3, v79
	v_mul_f32_e32 v52, v52, v80
	v_mul_f32_e32 v36, v36, v80
	v_mul_f32_e32 v20, v20, v80
	v_mul_f32_e32 v4, v4, v80
	v_mul_f32_e32 v53, v53, v81
	v_mul_f32_e32 v37, v37, v81
	v_mul_f32_e32 v21, v21, v81
	v_mul_f32_e32 v5, v5, v81
	v_mul_f32_e32 v54, v54, v74
	v_mul_f32_e32 v38, v38, v74
	v_mul_f32_e32 v22, v22, v74
	v_mul_f32_e32 v6, v6, v74
	v_mul_f32_e32 v55, v55, v75
	v_mul_f32_e32 v39, v39, v75
	v_mul_f32_e32 v23, v23, v75
	v_mul_f32_e32 v7, v7, v75
	v_mul_f32_e32 v56, v56, v76
	v_mul_f32_e32 v40, v40, v76
	v_mul_f32_e32 v24, v24, v76
	v_mul_f32_e32 v8, v8, v76
	v_mul_f32_e32 v57, v57, v77
	v_mul_f32_e32 v41, v41, v77
	v_mul_f32_e32 v25, v25, v77
	v_mul_f32_e32 v9, v9, v77
	v_mul_f32_e32 v58, v58, v70
	v_mul_f32_e32 v42, v42, v70
	v_mul_f32_e32 v26, v26, v70
	v_mul_f32_e32 v10, v10, v70
	v_mul_f32_e32 v59, v59, v71
	v_mul_f32_e32 v43, v43, v71
	v_mul_f32_e32 v27, v27, v71
	v_mul_f32_e32 v11, v11, v71
	v_mul_f32_e32 v60, v60, v72
	v_mul_f32_e32 v44, v44, v72
	v_mul_f32_e32 v28, v28, v72
	v_mul_f32_e32 v12, v12, v72
	v_mul_f32_e32 v61, v61, v73
	v_mul_f32_e32 v45, v45, v73
	v_mul_f32_e32 v29, v29, v73
	v_mul_f32_e32 v13, v13, v73
	v_mul_f32_e32 v62, v62, v66
	v_mul_f32_e32 v46, v46, v66
	v_mul_f32_e32 v30, v30, v66
	v_mul_f32_e32 v14, v14, v66
	v_mul_f32_e32 v63, v63, v67
	v_mul_f32_e32 v47, v47, v67
	v_mul_f32_e32 v31, v31, v67
	v_mul_f32_e32 v15, v15, v67
	v_mul_f32_e32 v64, v64, v68
	v_mul_f32_e32 v48, v48, v68
	v_mul_f32_e32 v32, v32, v68
	v_mul_f32_e32 v16, v16, v68
	v_mul_f32_e32 v65, v65, v69
	v_mul_f32_e32 v49, v49, v69
	v_mul_f32_e32 v33, v33, v69
	v_mul_f32_e32 v17, v17, v69
	v_and_b32_e32 v66, 1, v0
	v_cmp_eq_u32_e64 s[0:1], 0, v66
	v_and_b32_e32 v66, 2, v0
	v_cmp_eq_u32_e32 vcc, 0, v66
	v_and_b32_e32 v68, 3, v0
	v_mul_u32_u24_e32 v68, 0xffe, v68
	v_mov_b32_e32 v69, 0
	s_nop 0
	v_lshl_add_u64 v[70:71], v[82:83], 0, v[68:69]
	v_mov_b32_e32 v68, 0x8000
	v_cndmask_b32_e64 v66, v50, v51, s[0:1]
	v_cndmask_b32_e64 v72, v52, v53, s[0:1]
	s_nop 0
	v_mov_b32_dpp v67, v66 quad_perm:[1,0,3,2] row_mask:0xf bank_mask:0xf
	v_mov_b32_dpp v73, v72 quad_perm:[1,0,3,2] row_mask:0xf bank_mask:0xf
	v_cndmask_b32_e64 v50, v67, v50, s[0:1]
	v_cndmask_b32_e64 v51, v51, v67, s[0:1]
	v_cndmask_b32_e64 v52, v73, v52, s[0:1]
	v_cndmask_b32_e64 v53, v53, v73, s[0:1]
	v_cvt_pk_bf16_f32 v50, v50, v51
	v_cvt_pk_bf16_f32 v52, v52, v53
	s_nop 0
	v_cndmask_b32_e32 v66, v50, v52, vcc
	s_nop 1
	v_mov_b32_dpp v67, v66 quad_perm:[2,3,0,1] row_mask:0xf bank_mask:0xf
	s_nop 0
	v_cndmask_b32_e32 v50, v67, v50, vcc
	v_cndmask_b32_e32 v51, v52, v67, vcc
	global_store_dwordx2 v[70:71], v[50:51], off
	v_cndmask_b32_e64 v66, v34, v35, s[0:1]
	v_cndmask_b32_e64 v72, v36, v37, s[0:1]
	s_nop 0
	v_mov_b32_dpp v67, v66 quad_perm:[1,0,3,2] row_mask:0xf bank_mask:0xf
	v_mov_b32_dpp v73, v72 quad_perm:[1,0,3,2] row_mask:0xf bank_mask:0xf
	v_cndmask_b32_e64 v34, v67, v34, s[0:1]
	v_cndmask_b32_e64 v35, v35, v67, s[0:1]
	v_cndmask_b32_e64 v36, v73, v36, s[0:1]
	v_cndmask_b32_e64 v37, v37, v73, s[0:1]
	v_cvt_pk_bf16_f32 v34, v34, v35
	v_cvt_pk_bf16_f32 v36, v36, v37
	s_nop 0
	v_cndmask_b32_e32 v66, v34, v36, vcc
	s_nop 1
	v_mov_b32_dpp v67, v66 quad_perm:[2,3,0,1] row_mask:0xf bank_mask:0xf
	s_nop 0
	v_cndmask_b32_e32 v34, v67, v34, vcc
	v_cndmask_b32_e32 v35, v36, v67, vcc
	global_store_dwordx2 v[70:71], v[34:35], off offset:64
	v_cndmask_b32_e64 v66, v18, v19, s[0:1]
	v_cndmask_b32_e64 v72, v20, v21, s[0:1]
	s_nop 0
	v_mov_b32_dpp v67, v66 quad_perm:[1,0,3,2] row_mask:0xf bank_mask:0xf
	v_mov_b32_dpp v73, v72 quad_perm:[1,0,3,2] row_mask:0xf bank_mask:0xf
	v_cndmask_b32_e64 v18, v67, v18, s[0:1]
	v_cndmask_b32_e64 v19, v19, v67, s[0:1]
	v_cndmask_b32_e64 v20, v73, v20, s[0:1]
	v_cndmask_b32_e64 v21, v21, v73, s[0:1]
	v_cvt_pk_bf16_f32 v18, v18, v19
	v_cvt_pk_bf16_f32 v20, v20, v21
	s_nop 0
	v_cndmask_b32_e32 v66, v18, v20, vcc
	s_nop 1
	v_mov_b32_dpp v67, v66 quad_perm:[2,3,0,1] row_mask:0xf bank_mask:0xf
	s_nop 0
	v_cndmask_b32_e32 v18, v67, v18, vcc
; __device__ __forceinline__ int crow(int r, int hi) { return (r & 3) + 8 * (r >> 2) + 4 * hi; }
; template <class TIn, class TOut, int QS, int KS, int OS, bool BIAS, bool PREF = true>
; __device__ __forceinline__ void causal_swa_block(const BlockRef<TIn, TOut>& cur, const BlockRef<TIn, TOut>& nxt, int skv, int W, char* lds, Seam<TIn>& S) {
;     ...
;     for (int r = 0; r < 16; ++r) { const int orow = crow(r, hi);
; #pragma unroll
;         for (int d0 = 0; d0 < 4; ++d0) { const float v = o[d0][r] * rli[r];
;             if constexpr (same_t<TOut, float>::v) { Ow[(size_t)orow * OS + d0 * 32 + r32] = v; }
;             else { const float vn = __shfl_xor(v, 1);
;                    if ((r32 & 1) == 0) *(unsigned*)(Ow + (size_t)orow * OS + d0 * 32 + r32) = cvtpk(v, vn); } } }
	v_cndmask_b32_e32 v19, v20, v67, vcc
	global_store_dwordx2 v[70:71], v[18:19], off offset:128
	v_cndmask_b32_e64 v66, v2, v3, s[0:1]
	v_cndmask_b32_e64 v72, v4, v5, s[0:1]
	s_nop 0
	v_mov_b32_dpp v67, v66 quad_perm:[1,0,3,2] row_mask:0xf bank_mask:0xf
	v_mov_b32_dpp v73, v72 quad_perm:[1,0,3,2] row_mask:0xf bank_mask:0xf
	v_cndmask_b32_e64 v2, v67, v2, s[0:1]
	v_cndmask_b32_e64 v3, v3, v67, s[0:1]
	v_cndmask_b32_e64 v4, v73, v4, s[0:1]
	v_cndmask_b32_e64 v5, v5, v73, s[0:1]
	v_cvt_pk_bf16_f32 v2, v2, v3
	v_cvt_pk_bf16_f32 v4, v4, v5
	s_nop 0
	v_cndmask_b32_e32 v66, v2, v4, vcc
	s_nop 1
	v_mov_b32_dpp v67, v66 quad_perm:[2,3,0,1] row_mask:0xf bank_mask:0xf
	s_nop 0
	v_cndmask_b32_e32 v2, v67, v2, vcc
	v_cndmask_b32_e32 v3, v4, v67, vcc
	global_store_dwordx2 v[70:71], v[2:3], off offset:192
	v_lshl_add_u64 v[70:71], v[70:71], 0, v[68:69]
	v_cndmask_b32_e64 v66, v54, v55, s[0:1]
	v_cndmask_b32_e64 v72, v56, v57, s[0:1]
	s_nop 0
	v_mov_b32_dpp v67, v66 quad_perm:[1,0,3,2] row_mask:0xf bank_mask:0xf
	v_mov_b32_dpp v73, v72 quad_perm:[1,0,3,2] row_mask:0xf bank_mask:0xf
	v_cndmask_b32_e64 v54, v67, v54, s[0:1]
	v_cndmask_b32_e64 v55, v55, v67, s[0:1]
	v_cndmask_b32_e64 v56, v73, v56, s[0:1]
	v_cndmask_b32_e64 v57, v57, v73, s[0:1]
	v_cvt_pk_bf16_f32 v54, v54, v55
	v_cvt_pk_bf16_f32 v56, v56, v57
	s_nop 0
	v_cndmask_b32_e32 v66, v54, v56, vcc
	s_nop 1
	v_mov_b32_dpp v67, v66 quad_perm:[2,3,0,1] row_mask:0xf bank_mask:0xf
	s_nop 0
	v_cndmask_b32_e32 v54, v67, v54, vcc
	v_cndmask_b32_e32 v55, v56, v67, vcc
	global_store_dwordx2 v[70:71], v[54:55], off
	v_cndmask_b32_e64 v66, v38, v39, s[0:1]
	v_cndmask_b32_e64 v72, v40, v41, s[0:1]
	s_nop 0
	v_mov_b32_dpp v67, v66 quad_perm:[1,0,3,2] row_mask:0xf bank_mask:0xf
	v_mov_b32_dpp v73, v72 quad_perm:[1,0,3,2] row_mask:0xf bank_mask:0xf
	v_cndmask_b32_e64 v38, v67, v38, s[0:1]
	v_cndmask_b32_e64 v39, v39, v67, s[0:1]
	v_cndmask_b32_e64 v40, v73, v40, s[0:1]
	v_cndmask_b32_e64 v41, v41, v73, s[0:1]
	v_cvt_pk_bf16_f32 v38, v38, v39
	v_cvt_pk_bf16_f32 v40, v40, v41
	s_nop 0
	v_cndmask_b32_e32 v66, v38, v40, vcc
	s_nop 1
	v_mov_b32_dpp v67, v66 quad_perm:[2,3,0,1] row_mask:0xf bank_mask:0xf
	s_nop 0
	v_cndmask_b32_e32 v38, v67, v38, vcc
	v_cndmask_b32_e32 v39, v40, v67, vcc
	global_store_dwordx2 v[70:71], v[38:39], off offset:64
	v_cndmask_b32_e64 v66, v22, v23, s[0:1]
	v_cndmask_b32_e64 v72, v24, v25, s[0:1]
	s_nop 0
	v_mov_b32_dpp v67, v66 quad_perm:[1,0,3,2] row_mask:0xf bank_mask:0xf
	v_mov_b32_dpp v73, v72 quad_perm:[1,0,3,2] row_mask:0xf bank_mask:0xf
	v_cndmask_b32_e64 v22, v67, v22, s[0:1]
	v_cndmask_b32_e64 v23, v23, v67, s[0:1]
	v_cndmask_b32_e64 v24, v73, v24, s[0:1]
	v_cndmask_b32_e64 v25, v25, v73, s[0:1]
	v_cvt_pk_bf16_f32 v22, v22, v23
	v_cvt_pk_bf16_f32 v24, v24, v25
	s_nop 0
	v_cndmask_b32_e32 v66, v22, v24, vcc
	s_nop 1
	v_mov_b32_dpp v67, v66 quad_perm:[2,3,0,1] row_mask:0xf bank_mask:0xf
	s_nop 0
	v_cndmask_b32_e32 v22, v67, v22, vcc
	v_cndmask_b32_e32 v23, v24, v67, vcc
	global_store_dwordx2 v[70:71], v[22:23], off offset:128
	v_cndmask_b32_e64 v66, v6, v7, s[0:1]
	v_cndmask_b32_e64 v72, v8, v9, s[0:1]
	s_nop 0
	v_mov_b32_dpp v67, v66 quad_perm:[1,0,3,2] row_mask:0xf bank_mask:0xf
	v_mov_b32_dpp v73, v72 quad_perm:[1,0,3,2] row_mask:0xf bank_mask:0xf
	v_cndmask_b32_e64 v6, v67, v6, s[0:1]
	v_cndmask_b32_e64 v7, v7, v67, s[0:1]
	v_cndmask_b32_e64 v8, v73, v8, s[0:1]
	v_cndmask_b32_e64 v9, v9, v73, s[0:1]
	v_cvt_pk_bf16_f32 v6, v6, v7
	v_cvt_pk_bf16_f32 v8, v8, v9
	s_nop 0
	v_cndmask_b32_e32 v66, v6, v8, vcc
	s_nop 1
	v_mov_b32_dpp v67, v66 quad_perm:[2,3,0,1] row_mask:0xf bank_mask:0xf
	s_nop 0
	v_cndmask_b32_e32 v6, v67, v6, vcc
	v_cndmask_b32_e32 v7, v8, v67, vcc
	global_store_dwordx2 v[70:71], v[6:7], off offset:192
	v_lshl_add_u64 v[70:71], v[70:71], 0, v[68:69]
	v_cndmask_b32_e64 v66, v58, v59, s[0:1]
	v_cndmask_b32_e64 v72, v60, v61, s[0:1]
	s_nop 0
	v_mov_b32_dpp v67, v66 quad_perm:[1,0,3,2] row_mask:0xf bank_mask:0xf
	v_mov_b32_dpp v73, v72 quad_perm:[1,0,3,2] row_mask:0xf bank_mask:0xf
	v_cndmask_b32_e64 v58, v67, v58, s[0:1]
	v_cndmask_b32_e64 v59, v59, v67, s[0:1]
	v_cndmask_b32_e64 v60, v73, v60, s[0:1]
	v_cndmask_b32_e64 v61, v61, v73, s[0:1]
	v_cvt_pk_bf16_f32 v58, v58, v59
	v_cvt_pk_bf16_f32 v60, v60, v61
	s_nop 0
	v_cndmask_b32_e32 v66, v58, v60, vcc
	s_nop 1
	v_mov_b32_dpp v67, v66 quad_perm:[2,3,0,1] row_mask:0xf bank_mask:0xf
	s_nop 0
	v_cndmask_b32_e32 v58, v67, v58, vcc
	v_cndmask_b32_e32 v59, v60, v67, vcc
	global_store_dwordx2 v[70:71], v[58:59], off
	v_cndmask_b32_e64 v66, v42, v43, s[0:1]
	v_cndmask_b32_e64 v72, v44, v45, s[0:1]
	s_nop 0
	v_mov_b32_dpp v67, v66 quad_perm:[1,0,3,2] row_mask:0xf bank_mask:0xf
	v_mov_b32_dpp v73, v72 quad_perm:[1,0,3,2] row_mask:0xf bank_mask:0xf
	v_cndmask_b32_e64 v42, v67, v42, s[0:1]
	v_cndmask_b32_e64 v43, v43, v67, s[0:1]
	v_cndmask_b32_e64 v44, v73, v44, s[0:1]
	v_cndmask_b32_e64 v45, v45, v73, s[0:1]
	v_cvt_pk_bf16_f32 v42, v42, v43
	v_cvt_pk_bf16_f32 v44, v44, v45
	s_nop 0
	v_cndmask_b32_e32 v66, v42, v44, vcc
	s_nop 1
	v_mov_b32_dpp v67, v66 quad_perm:[2,3,0,1] row_mask:0xf bank_mask:0xf
	s_nop 0
	v_cndmask_b32_e32 v42, v67, v42, vcc
	v_cndmask_b32_e32 v43, v44, v67, vcc
	global_store_dwordx2 v[70:71], v[42:43], off offset:64
	v_cndmask_b32_e64 v66, v26, v27, s[0:1]
; #define SBAR() __builtin_amdgcn_sched_barrier(0)
; __device__ __forceinline__ int crow(int r, int hi) { return (r & 3) + 8 * (r >> 2) + 4 * hi; }
; #define VMW() asm volatile("s_waitcnt vmcnt(0)" ::: "memory")
; #define SLOAD_H(Kp, Vp, k0) do { S.st_v0 = load8<TIn>(ROW(Vp, k0, sr)); S.st_v1 = load8<TIn>(ROW(Vp, k0, 32 + sr));              \
;                          S.st_k0 = load8<TIn>(ROW(Kp, k0, sr)); S.st_k1 = load8<TIn>(ROW(Kp, k0, 32 + sr)); } while (0)
; #define SWRITE_HV(bf) do { *(bf16x8*)(V_lds + (bf) * SHM_V + vst0) = S.st_v0; *(bf16x8*)(V_lds + (bf) * SHM_V + vst1) = S.st_v1; } while (0)
; #define SLOAD_F(p, k0) do { S.sf0 = *(const f32x4*)ROW(p, k0, sr); S.sf1 = *(const f32x4*)(ROW(p, k0, sr) + 4);                \
;                             S.sf2 = *(const f32x4*)ROW(p, k0, 32 + sr); S.sf3 = *(const f32x4*)(ROW(p, k0, 32 + sr) + 4); } while (0)
; #define SWRITE_VF(bf) do { *(bf16x8*)(V_lds + (bf) * SHM_V + vst0) = pack8(S.sf0, S.sf1); *(bf16x8*)(V_lds + (bf) * SHM_V + vst1) = pack8(S.sf2, S.sf3); } while (0)
; template <class TIn, class TOut, int QS, int KS, int OS, bool BIAS, bool PREF = true>
; __device__ __forceinline__ void causal_swa_block(const BlockRef<TIn, TOut>& cur, const BlockRef<TIn, TOut>& nxt, int skv, int W, char* lds, Seam<TIn>& S) {
;     ...
;     if constexpr (F32) { VMW(); SWRITE_VF(0); SBAR(); } else { SWRITE_HV(0); SBAR(); }
;     if (NT > 1) { if constexpr (F32) SLOAD_F((const float*)Kh, KBASE(1)); else SLOAD_H(Kh, Vh, KBASE(1)); }
;     ...
;     for (int r = 0; r < 16; ++r) { const int orow = crow(r, hi);
; #pragma unroll
;         for (int d0 = 0; d0 < 4; ++d0) { const float v = o[d0][r] * rli[r];
;             if constexpr (same_t<TOut, float>::v) { Ow[(size_t)orow * OS + d0 * 32 + r32] = v; }
;             else { const float vn = __shfl_xor(v, 1);
;                    if ((r32 & 1) == 0) *(unsigned*)(Ow + (size_t)orow * OS + d0 * 32 + r32) = cvtpk(v, vn); } } }
	v_cndmask_b32_e64 v72, v28, v29, s[0:1]
	s_nop 0
	v_mov_b32_dpp v67, v66 quad_perm:[1,0,3,2] row_mask:0xf bank_mask:0xf
	v_mov_b32_dpp v73, v72 quad_perm:[1,0,3,2] row_mask:0xf bank_mask:0xf
	v_cndmask_b32_e64 v26, v67, v26, s[0:1]
	v_cndmask_b32_e64 v27, v27, v67, s[0:1]
	v_cndmask_b32_e64 v28, v73, v28, s[0:1]
	v_cndmask_b32_e64 v29, v29, v73, s[0:1]
	v_cvt_pk_bf16_f32 v26, v26, v27
	v_cvt_pk_bf16_f32 v28, v28, v29
	s_nop 0
	v_cndmask_b32_e32 v66, v26, v28, vcc
	s_nop 1
	v_mov_b32_dpp v67, v66 quad_perm:[2,3,0,1] row_mask:0xf bank_mask:0xf
	s_nop 0
	v_cndmask_b32_e32 v26, v67, v26, vcc
	v_cndmask_b32_e32 v27, v28, v67, vcc
	global_store_dwordx2 v[70:71], v[26:27], off offset:128
	v_cndmask_b32_e64 v66, v10, v11, s[0:1]
	v_cndmask_b32_e64 v72, v12, v13, s[0:1]
	s_nop 0
	v_mov_b32_dpp v67, v66 quad_perm:[1,0,3,2] row_mask:0xf bank_mask:0xf
	v_mov_b32_dpp v73, v72 quad_perm:[1,0,3,2] row_mask:0xf bank_mask:0xf
	v_cndmask_b32_e64 v10, v67, v10, s[0:1]
	v_cndmask_b32_e64 v11, v11, v67, s[0:1]
	v_cndmask_b32_e64 v12, v73, v12, s[0:1]
	v_cndmask_b32_e64 v13, v13, v73, s[0:1]
	v_cvt_pk_bf16_f32 v10, v10, v11
	v_cvt_pk_bf16_f32 v12, v12, v13
	s_nop 0
	v_cndmask_b32_e32 v66, v10, v12, vcc
	s_nop 1
	v_mov_b32_dpp v67, v66 quad_perm:[2,3,0,1] row_mask:0xf bank_mask:0xf
	s_nop 0
	v_cndmask_b32_e32 v10, v67, v10, vcc
	v_cndmask_b32_e32 v11, v12, v67, vcc
	global_store_dwordx2 v[70:71], v[10:11], off offset:192
	v_lshl_add_u64 v[70:71], v[70:71], 0, v[68:69]
	v_cndmask_b32_e64 v66, v62, v63, s[0:1]
	v_cndmask_b32_e64 v72, v64, v65, s[0:1]
	s_nop 0
	v_mov_b32_dpp v67, v66 quad_perm:[1,0,3,2] row_mask:0xf bank_mask:0xf
	v_mov_b32_dpp v73, v72 quad_perm:[1,0,3,2] row_mask:0xf bank_mask:0xf
	v_cndmask_b32_e64 v62, v67, v62, s[0:1]
	v_cndmask_b32_e64 v63, v63, v67, s[0:1]
	v_cndmask_b32_e64 v64, v73, v64, s[0:1]
	v_cndmask_b32_e64 v65, v65, v73, s[0:1]
	v_cvt_pk_bf16_f32 v62, v62, v63
	v_cvt_pk_bf16_f32 v64, v64, v65
	s_nop 0
	v_cndmask_b32_e32 v66, v62, v64, vcc
	s_nop 1
	v_mov_b32_dpp v67, v66 quad_perm:[2,3,0,1] row_mask:0xf bank_mask:0xf
	s_nop 0
	v_cndmask_b32_e32 v62, v67, v62, vcc
	v_cndmask_b32_e32 v63, v64, v67, vcc
	global_store_dwordx2 v[70:71], v[62:63], off
	v_cndmask_b32_e64 v66, v46, v47, s[0:1]
	v_cndmask_b32_e64 v72, v48, v49, s[0:1]
	s_nop 0
	v_mov_b32_dpp v67, v66 quad_perm:[1,0,3,2] row_mask:0xf bank_mask:0xf
	v_mov_b32_dpp v73, v72 quad_perm:[1,0,3,2] row_mask:0xf bank_mask:0xf
	v_cndmask_b32_e64 v46, v67, v46, s[0:1]
	v_cndmask_b32_e64 v47, v47, v67, s[0:1]
	v_cndmask_b32_e64 v48, v73, v48, s[0:1]
	v_cndmask_b32_e64 v49, v49, v73, s[0:1]
	v_cvt_pk_bf16_f32 v46, v46, v47
	v_cvt_pk_bf16_f32 v48, v48, v49
	s_nop 0
	v_cndmask_b32_e32 v66, v46, v48, vcc
	s_nop 1
	v_mov_b32_dpp v67, v66 quad_perm:[2,3,0,1] row_mask:0xf bank_mask:0xf
	s_nop 0
	v_cndmask_b32_e32 v46, v67, v46, vcc
	v_cndmask_b32_e32 v47, v48, v67, vcc
	global_store_dwordx2 v[70:71], v[46:47], off offset:64
	v_cndmask_b32_e64 v66, v30, v31, s[0:1]
	v_cndmask_b32_e64 v72, v32, v33, s[0:1]
	s_nop 0
	v_mov_b32_dpp v67, v66 quad_perm:[1,0,3,2] row_mask:0xf bank_mask:0xf
	v_mov_b32_dpp v73, v72 quad_perm:[1,0,3,2] row_mask:0xf bank_mask:0xf
	v_cndmask_b32_e64 v30, v67, v30, s[0:1]
	v_cndmask_b32_e64 v31, v31, v67, s[0:1]
	v_cndmask_b32_e64 v32, v73, v32, s[0:1]
	v_cndmask_b32_e64 v33, v33, v73, s[0:1]
	v_cvt_pk_bf16_f32 v30, v30, v31
	v_cvt_pk_bf16_f32 v32, v32, v33
	s_nop 0
	v_cndmask_b32_e32 v66, v30, v32, vcc
	s_nop 1
	v_mov_b32_dpp v67, v66 quad_perm:[2,3,0,1] row_mask:0xf bank_mask:0xf
	s_nop 0
	v_cndmask_b32_e32 v30, v67, v30, vcc
	v_cndmask_b32_e32 v31, v32, v67, vcc
	global_store_dwordx2 v[70:71], v[30:31], off offset:128
	v_cndmask_b32_e64 v66, v14, v15, s[0:1]
	v_cndmask_b32_e64 v72, v16, v17, s[0:1]
	s_nop 0
	v_mov_b32_dpp v67, v66 quad_perm:[1,0,3,2] row_mask:0xf bank_mask:0xf
	v_mov_b32_dpp v73, v72 quad_perm:[1,0,3,2] row_mask:0xf bank_mask:0xf
	v_cndmask_b32_e64 v14, v67, v14, s[0:1]
	v_cndmask_b32_e64 v15, v15, v67, s[0:1]
	v_cndmask_b32_e64 v16, v73, v16, s[0:1]
	v_cndmask_b32_e64 v17, v17, v73, s[0:1]
	v_cvt_pk_bf16_f32 v14, v14, v15
	v_cvt_pk_bf16_f32 v16, v16, v17
	s_nop 0
	v_cndmask_b32_e32 v66, v14, v16, vcc
	s_nop 1
	v_mov_b32_dpp v67, v66 quad_perm:[2,3,0,1] row_mask:0xf bank_mask:0xf
	s_nop 0
	v_cndmask_b32_e32 v14, v67, v14, vcc
	v_cndmask_b32_e32 v15, v16, v67, vcc
	global_store_dwordx2 v[70:71], v[14:15], off offset:192
	v_readfirstlane_b32 s19, v0
	s_lshr_b32 s1, s19, 1
	s_and_b32 s14, s1, 0x7fffffe0
	s_add_i32 s30, s14, s31
	v_or_b32_e32 v2, s30, v216
	s_waitcnt lgkmcnt(0)
	v_lshl_add_u32 v3, v2, 2, 0
	v_add_u32_e32 v3, 0x10800, v3
	s_waitcnt vmcnt(63) expcnt(7) lgkmcnt(15)
	s_barrier
	ds_read_b32 v35, v3
	s_lshr_b32 s15, s31, 6
	s_lshr_b32 s0, s18, 6
	s_add_i32 s15, s15, 4
	s_sub_i32 s31, s15, s0
	s_mov_b32 s1, 0
	ds_write_b128 v213, v[98:101]
	ds_write_b128 v214, v[110:113]
	s_cmp_gt_i32 s31, 1
	s_cselect_b64 s[16:17], -1, 0
	s_cmp_lt_i32 s31, 2
	s_cbranch_scc1 .LBB0_635
	s_add_i32 s0, s18, 64
	s_lshl_b64 s[0:1], s[0:1], 11
	s_add_u32 s26, s26, s0
	s_addc_u32 s27, s27, s1
	s_add_u32 s0, s22, s0
	s_addc_u32 s1, s25, s1
	global_load_dwordx4 v[98:101], v194, s[26:27]
	global_load_dwordx4 v[102:105], v194, s[0:1]
	global_load_dwordx4 v[110:113], v204, s[26:27]
	global_load_dwordx4 v[106:109], v204, s[0:1]

; __device__ __forceinline__ int crow(int r, int hi) { return (r & 3) + 8 * (r >> 2) + 4 * hi; }
; template <class TIn, class TOut, int QS, int KS, int OS, bool BIAS, bool PREF = true>
; __device__ __forceinline__ void causal_swa_block(const BlockRef<TIn, TOut>& cur, const BlockRef<TIn, TOut>& nxt, int skv, int W, char* lds, Seam<TIn>& S) {
;     ...
;     if (hi == 0) li_l[r32] = l_reg; asm volatile("s_waitcnt lgkmcnt(0)" ::: "memory");
;     float rli[16];
; #pragma unroll
;     for (int r = 0; r < 16; ++r) rli[r] = __builtin_amdgcn_rcpf(li_l[crow(r, hi)]);
;     TOut* Ow = cur.O + (size_t)(wid * QBLK) * OS;
; #pragma unroll
;     for (int r = 0; r < 16; ++r) { const int orow = crow(r, hi);
; #pragma unroll
;         for (int d0 = 0; d0 < 4; ++d0) { const float v = o[d0][r] * rli[r];
;             if constexpr (same_t<TOut, float>::v) { Ow[(size_t)orow * OS + d0 * 32 + r32] = v; }
;             else { const float vn = __shfl_xor(v, 1);
;                    if ((r32 & 1) == 0) *(unsigned*)(Ow + (size_t)orow * OS + d0 * 32 + r32) = cvtpk(v, vn); } } }
.LBB0_669:
	s_and_saveexec_b64 s[0:1], s[4:5]
	ds_write_b32 v218, v98
	s_or_b64 exec, exec, s[0:1]
	s_waitcnt lgkmcnt(0)
	ds_read_b128 v[78:81], v201
	ds_read_b128 v[74:77], v201 offset:32
	s_lshl_b64 s[0:1], s[12:13], 12
	s_add_u32 s0, s29, s0
	s_addc_u32 s1, s28, s1
	s_waitcnt lgkmcnt(1)
	s_add_u32 s4, s0, s10
	s_mov_b32 s15, 0
	s_addc_u32 s5, s1, s11
	ds_read_b128 v[70:73], v201 offset:64
	ds_read_b128 v[66:69], v201 offset:96
	s_lshl_b64 s[0:1], s[14:15], 12
	s_add_u32 s0, s4, s0
	s_addc_u32 s1, s5, s1
	v_mov_b32_e32 v201, 0
	v_lshl_add_u64 v[82:83], s[0:1], 0, v[200:201]
	v_lshl_add_u64 v[82:83], v[82:83], 0, v[202:203]
	s_waitcnt lgkmcnt(0)
	v_rcp_f32_e32 v78, v78
	v_rcp_f32_e32 v79, v79
	v_rcp_f32_e32 v80, v80
	v_rcp_f32_e32 v81, v81
	v_rcp_f32_e32 v74, v74
	v_rcp_f32_e32 v75, v75
	v_rcp_f32_e32 v76, v76
	v_rcp_f32_e32 v77, v77
	v_rcp_f32_e32 v70, v70
	v_rcp_f32_e32 v71, v71
	v_rcp_f32_e32 v72, v72
	v_rcp_f32_e32 v73, v73
	v_rcp_f32_e32 v66, v66
	v_rcp_f32_e32 v67, v67
	v_rcp_f32_e32 v68, v68
	v_rcp_f32_e32 v69, v69
	v_mul_f32_e32 v50, v50, v78
	v_mul_f32_e32 v34, v34, v78
	v_mul_f32_e32 v18, v18, v78
	v_mul_f32_e32 v2, v2, v78
	v_mul_f32_e32 v51, v51, v79
	v_mul_f32_e32 v35, v35, v79
	v_mul_f32_e32 v19, v19, v79
	v_mul_f32_e32 v3, v3, v79
	v_mul_f32_e32 v52, v52, v80
	v_mul_f32_e32 v36, v36, v80
	v_mul_f32_e32 v20, v20, v80
	v_mul_f32_e32 v4, v4, v80
	v_mul_f32_e32 v53, v53, v81
	v_mul_f32_e32 v37, v37, v81
	v_mul_f32_e32 v21, v21, v81
	v_mul_f32_e32 v5, v5, v81
	v_mul_f32_e32 v54, v54, v74
	v_mul_f32_e32 v38, v38, v74
	v_mul_f32_e32 v22, v22, v74
	v_mul_f32_e32 v6, v6, v74
	v_mul_f32_e32 v55, v55, v75
	v_mul_f32_e32 v39, v39, v75
	v_mul_f32_e32 v23, v23, v75
	v_mul_f32_e32 v7, v7, v75
	v_mul_f32_e32 v56, v56, v76
	v_mul_f32_e32 v40, v40, v76
	v_mul_f32_e32 v24, v24, v76
	v_mul_f32_e32 v8, v8, v76
	v_mul_f32_e32 v57, v57, v77
	v_mul_f32_e32 v41, v41, v77
	v_mul_f32_e32 v25, v25, v77
	v_mul_f32_e32 v9, v9, v77
	v_mul_f32_e32 v58, v58, v70
	v_mul_f32_e32 v42, v42, v70
	v_mul_f32_e32 v26, v26, v70
	v_mul_f32_e32 v10, v10, v70
	v_mul_f32_e32 v59, v59, v71
	v_mul_f32_e32 v43, v43, v71
	v_mul_f32_e32 v27, v27, v71
	v_mul_f32_e32 v11, v11, v71
	v_mul_f32_e32 v60, v60, v72
	v_mul_f32_e32 v44, v44, v72
	v_mul_f32_e32 v28, v28, v72
	v_mul_f32_e32 v12, v12, v72
	v_mul_f32_e32 v61, v61, v73
	v_mul_f32_e32 v45, v45, v73
	v_mul_f32_e32 v29, v29, v73
	v_mul_f32_e32 v13, v13, v73
	v_mul_f32_e32 v62, v62, v66
	v_mul_f32_e32 v46, v46, v66
	v_mul_f32_e32 v30, v30, v66
	v_mul_f32_e32 v14, v14, v66
	v_mul_f32_e32 v63, v63, v67
	v_mul_f32_e32 v47, v47, v67
	v_mul_f32_e32 v31, v31, v67
	v_mul_f32_e32 v15, v15, v67
	v_mul_f32_e32 v64, v64, v68
	v_mul_f32_e32 v48, v48, v68
	v_mul_f32_e32 v32, v32, v68
	v_mul_f32_e32 v16, v16, v68
	v_mul_f32_e32 v65, v65, v69
	v_mul_f32_e32 v49, v49, v69
	v_mul_f32_e32 v33, v33, v69
	v_mul_f32_e32 v17, v17, v69
	v_and_b32_e32 v66, 1, v0
	v_cmp_eq_u32_e64 s[0:1], 0, v66
	v_and_b32_e32 v66, 2, v0
	v_cmp_eq_u32_e32 vcc, 0, v66
	v_and_b32_e32 v68, 3, v0
	v_mul_u32_u24_e32 v68, 0xffe, v68
	v_mov_b32_e32 v69, 0
	s_nop 0
	v_lshl_add_u64 v[70:71], v[82:83], 0, v[68:69]
	v_mov_b32_e32 v68, 0x8000
	v_cndmask_b32_e64 v66, v50, v51, s[0:1]
	v_cndmask_b32_e64 v72, v52, v53, s[0:1]
	s_nop 0
	v_mov_b32_dpp v67, v66 quad_perm:[1,0,3,2] row_mask:0xf bank_mask:0xf
	v_mov_b32_dpp v73, v72 quad_perm:[1,0,3,2] row_mask:0xf bank_mask:0xf
	v_cndmask_b32_e64 v50, v67, v50, s[0:1]
	v_cndmask_b32_e64 v51, v51, v67, s[0:1]
	v_cndmask_b32_e64 v52, v73, v52, s[0:1]
	v_cndmask_b32_e64 v53, v53, v73, s[0:1]
	v_cvt_pk_bf16_f32 v50, v50, v51
	v_cvt_pk_bf16_f32 v52, v52, v53
	s_nop 0
	v_cndmask_b32_e32 v66, v50, v52, vcc
	s_nop 1
	v_mov_b32_dpp v67, v66 quad_perm:[2,3,0,1] row_mask:0xf bank_mask:0xf
	s_nop 0
	v_cndmask_b32_e32 v50, v67, v50, vcc
	v_cndmask_b32_e32 v51, v52, v67, vcc
	global_store_dwordx2 v[70:71], v[50:51], off
	v_cndmask_b32_e64 v66, v34, v35, s[0:1]
	v_cndmask_b32_e64 v72, v36, v37, s[0:1]
	s_nop 0
	v_mov_b32_dpp v67, v66 quad_perm:[1,0,3,2] row_mask:0xf bank_mask:0xf
	v_mov_b32_dpp v73, v72 quad_perm:[1,0,3,2] row_mask:0xf bank_mask:0xf
	v_cndmask_b32_e64 v34, v67, v34, s[0:1]
	v_cndmask_b32_e64 v35, v35, v67, s[0:1]
	v_cndmask_b32_e64 v36, v73, v36, s[0:1]
	v_cndmask_b32_e64 v37, v37, v73, s[0:1]
	v_cvt_pk_bf16_f32 v34, v34, v35
	v_cvt_pk_bf16_f32 v36, v36, v37
	s_nop 0
	v_cndmask_b32_e32 v66, v34, v36, vcc
	s_nop 1
	v_mov_b32_dpp v67, v66 quad_perm:[2,3,0,1] row_mask:0xf bank_mask:0xf
	s_nop 0
	v_cndmask_b32_e32 v34, v67, v34, vcc
	v_cndmask_b32_e32 v35, v36, v67, vcc
	global_store_dwordx2 v[70:71], v[34:35], off offset:64
	v_cndmask_b32_e64 v66, v18, v19, s[0:1]
	v_cndmask_b32_e64 v72, v20, v21, s[0:1]
	s_nop 0
	v_mov_b32_dpp v67, v66 quad_perm:[1,0,3,2] row_mask:0xf bank_mask:0xf
	v_mov_b32_dpp v73, v72 quad_perm:[1,0,3,2] row_mask:0xf bank_mask:0xf
	v_cndmask_b32_e64 v18, v67, v18, s[0:1]
	v_cndmask_b32_e64 v19, v19, v67, s[0:1]
	v_cndmask_b32_e64 v20, v73, v20, s[0:1]
	v_cndmask_b32_e64 v21, v21, v73, s[0:1]
	v_cvt_pk_bf16_f32 v18, v18, v19
	v_cvt_pk_bf16_f32 v20, v20, v21
	s_nop 0
	v_cndmask_b32_e32 v66, v18, v20, vcc
	s_nop 1
	v_mov_b32_dpp v67, v66 quad_perm:[2,3,0,1] row_mask:0xf bank_mask:0xf
	s_nop 0
	v_cndmask_b32_e32 v18, v67, v18, vcc
	v_cndmask_b32_e32 v19, v20, v67, vcc
	global_store_dwordx2 v[70:71], v[18:19], off offset:128
	v_cndmask_b32_e64 v66, v2, v3, s[0:1]
	v_cndmask_b32_e64 v72, v4, v5, s[0:1]
	s_nop 0
	v_mov_b32_dpp v67, v66 quad_perm:[1,0,3,2] row_mask:0xf bank_mask:0xf
	v_mov_b32_dpp v73, v72 quad_perm:[1,0,3,2] row_mask:0xf bank_mask:0xf
	v_cndmask_b32_e64 v2, v67, v2, s[0:1]
	v_cndmask_b32_e64 v3, v3, v67, s[0:1]
; __device__ __forceinline__ int crow(int r, int hi) { return (r & 3) + 8 * (r >> 2) + 4 * hi; }
; template <class TIn, class TOut, int QS, int KS, int OS, bool BIAS, bool PREF = true>
; __device__ __forceinline__ void causal_swa_block(const BlockRef<TIn, TOut>& cur, const BlockRef<TIn, TOut>& nxt, int skv, int W, char* lds, Seam<TIn>& S) {
;     ...
;     for (int r = 0; r < 16; ++r) { const int orow = crow(r, hi);
; #pragma unroll
;         for (int d0 = 0; d0 < 4; ++d0) { const float v = o[d0][r] * rli[r];
;             if constexpr (same_t<TOut, float>::v) { Ow[(size_t)orow * OS + d0 * 32 + r32] = v; }
;             else { const float vn = __shfl_xor(v, 1);
;                    if ((r32 & 1) == 0) *(unsigned*)(Ow + (size_t)orow * OS + d0 * 32 + r32) = cvtpk(v, vn); } } }
	v_cndmask_b32_e64 v4, v73, v4, s[0:1]
	v_cndmask_b32_e64 v5, v5, v73, s[0:1]
	v_cvt_pk_bf16_f32 v2, v2, v3
	v_cvt_pk_bf16_f32 v4, v4, v5
	s_nop 0
	v_cndmask_b32_e32 v66, v2, v4, vcc
	s_nop 1
	v_mov_b32_dpp v67, v66 quad_perm:[2,3,0,1] row_mask:0xf bank_mask:0xf
	s_nop 0
	v_cndmask_b32_e32 v2, v67, v2, vcc
	v_cndmask_b32_e32 v3, v4, v67, vcc
	global_store_dwordx2 v[70:71], v[2:3], off offset:192
	v_lshl_add_u64 v[70:71], v[70:71], 0, v[68:69]
	v_cndmask_b32_e64 v66, v54, v55, s[0:1]
	v_cndmask_b32_e64 v72, v56, v57, s[0:1]
	s_nop 0
	v_mov_b32_dpp v67, v66 quad_perm:[1,0,3,2] row_mask:0xf bank_mask:0xf
	v_mov_b32_dpp v73, v72 quad_perm:[1,0,3,2] row_mask:0xf bank_mask:0xf
	v_cndmask_b32_e64 v54, v67, v54, s[0:1]
	v_cndmask_b32_e64 v55, v55, v67, s[0:1]
	v_cndmask_b32_e64 v56, v73, v56, s[0:1]
	v_cndmask_b32_e64 v57, v57, v73, s[0:1]
	v_cvt_pk_bf16_f32 v54, v54, v55
	v_cvt_pk_bf16_f32 v56, v56, v57
	s_nop 0
	v_cndmask_b32_e32 v66, v54, v56, vcc
	s_nop 1
	v_mov_b32_dpp v67, v66 quad_perm:[2,3,0,1] row_mask:0xf bank_mask:0xf
	s_nop 0
	v_cndmask_b32_e32 v54, v67, v54, vcc
	v_cndmask_b32_e32 v55, v56, v67, vcc
	global_store_dwordx2 v[70:71], v[54:55], off
	v_cndmask_b32_e64 v66, v38, v39, s[0:1]
	v_cndmask_b32_e64 v72, v40, v41, s[0:1]
	s_nop 0
	v_mov_b32_dpp v67, v66 quad_perm:[1,0,3,2] row_mask:0xf bank_mask:0xf
	v_mov_b32_dpp v73, v72 quad_perm:[1,0,3,2] row_mask:0xf bank_mask:0xf
	v_cndmask_b32_e64 v38, v67, v38, s[0:1]
	v_cndmask_b32_e64 v39, v39, v67, s[0:1]
	v_cndmask_b32_e64 v40, v73, v40, s[0:1]
	v_cndmask_b32_e64 v41, v41, v73, s[0:1]
	v_cvt_pk_bf16_f32 v38, v38, v39
	v_cvt_pk_bf16_f32 v40, v40, v41
	s_nop 0
	v_cndmask_b32_e32 v66, v38, v40, vcc
	s_nop 1
	v_mov_b32_dpp v67, v66 quad_perm:[2,3,0,1] row_mask:0xf bank_mask:0xf
	s_nop 0
	v_cndmask_b32_e32 v38, v67, v38, vcc
	v_cndmask_b32_e32 v39, v40, v67, vcc
	global_store_dwordx2 v[70:71], v[38:39], off offset:64
	v_cndmask_b32_e64 v66, v22, v23, s[0:1]
	v_cndmask_b32_e64 v72, v24, v25, s[0:1]
	s_nop 0
	v_mov_b32_dpp v67, v66 quad_perm:[1,0,3,2] row_mask:0xf bank_mask:0xf
	v_mov_b32_dpp v73, v72 quad_perm:[1,0,3,2] row_mask:0xf bank_mask:0xf
	v_cndmask_b32_e64 v22, v67, v22, s[0:1]
	v_cndmask_b32_e64 v23, v23, v67, s[0:1]
	v_cndmask_b32_e64 v24, v73, v24, s[0:1]
	v_cndmask_b32_e64 v25, v25, v73, s[0:1]
	v_cvt_pk_bf16_f32 v22, v22, v23
	v_cvt_pk_bf16_f32 v24, v24, v25
	s_nop 0
	v_cndmask_b32_e32 v66, v22, v24, vcc
	s_nop 1
	v_mov_b32_dpp v67, v66 quad_perm:[2,3,0,1] row_mask:0xf bank_mask:0xf
	s_nop 0
	v_cndmask_b32_e32 v22, v67, v22, vcc
	v_cndmask_b32_e32 v23, v24, v67, vcc
	global_store_dwordx2 v[70:71], v[22:23], off offset:128
	v_cndmask_b32_e64 v66, v6, v7, s[0:1]
	v_cndmask_b32_e64 v72, v8, v9, s[0:1]
	s_nop 0
	v_mov_b32_dpp v67, v66 quad_perm:[1,0,3,2] row_mask:0xf bank_mask:0xf
	v_mov_b32_dpp v73, v72 quad_perm:[1,0,3,2] row_mask:0xf bank_mask:0xf
	v_cndmask_b32_e64 v6, v67, v6, s[0:1]
	v_cndmask_b32_e64 v7, v7, v67, s[0:1]
	v_cndmask_b32_e64 v8, v73, v8, s[0:1]
	v_cndmask_b32_e64 v9, v9, v73, s[0:1]
	v_cvt_pk_bf16_f32 v6, v6, v7
	v_cvt_pk_bf16_f32 v8, v8, v9
	s_nop 0
	v_cndmask_b32_e32 v66, v6, v8, vcc
	s_nop 1
	v_mov_b32_dpp v67, v66 quad_perm:[2,3,0,1] row_mask:0xf bank_mask:0xf
	s_nop 0
	v_cndmask_b32_e32 v6, v67, v6, vcc
	v_cndmask_b32_e32 v7, v8, v67, vcc
	global_store_dwordx2 v[70:71], v[6:7], off offset:192
	v_lshl_add_u64 v[70:71], v[70:71], 0, v[68:69]
	v_cndmask_b32_e64 v66, v58, v59, s[0:1]
	v_cndmask_b32_e64 v72, v60, v61, s[0:1]
	s_nop 0
	v_mov_b32_dpp v67, v66 quad_perm:[1,0,3,2] row_mask:0xf bank_mask:0xf
	v_mov_b32_dpp v73, v72 quad_perm:[1,0,3,2] row_mask:0xf bank_mask:0xf
	v_cndmask_b32_e64 v58, v67, v58, s[0:1]
	v_cndmask_b32_e64 v59, v59, v67, s[0:1]
	v_cndmask_b32_e64 v60, v73, v60, s[0:1]
	v_cndmask_b32_e64 v61, v61, v73, s[0:1]
	v_cvt_pk_bf16_f32 v58, v58, v59
	v_cvt_pk_bf16_f32 v60, v60, v61
	s_nop 0
	v_cndmask_b32_e32 v66, v58, v60, vcc
	s_nop 1
	v_mov_b32_dpp v67, v66 quad_perm:[2,3,0,1] row_mask:0xf bank_mask:0xf
	s_nop 0
	v_cndmask_b32_e32 v58, v67, v58, vcc
	v_cndmask_b32_e32 v59, v60, v67, vcc
	global_store_dwordx2 v[70:71], v[58:59], off
	v_cndmask_b32_e64 v66, v42, v43, s[0:1]
	v_cndmask_b32_e64 v72, v44, v45, s[0:1]
	s_nop 0
	v_mov_b32_dpp v67, v66 quad_perm:[1,0,3,2] row_mask:0xf bank_mask:0xf
	v_mov_b32_dpp v73, v72 quad_perm:[1,0,3,2] row_mask:0xf bank_mask:0xf
	v_cndmask_b32_e64 v42, v67, v42, s[0:1]
	v_cndmask_b32_e64 v43, v43, v67, s[0:1]
	v_cndmask_b32_e64 v44, v73, v44, s[0:1]
	v_cndmask_b32_e64 v45, v45, v73, s[0:1]
	v_cvt_pk_bf16_f32 v42, v42, v43
	v_cvt_pk_bf16_f32 v44, v44, v45
	s_nop 0
	v_cndmask_b32_e32 v66, v42, v44, vcc
	s_nop 1
	v_mov_b32_dpp v67, v66 quad_perm:[2,3,0,1] row_mask:0xf bank_mask:0xf
	s_nop 0
	v_cndmask_b32_e32 v42, v67, v42, vcc
	v_cndmask_b32_e32 v43, v44, v67, vcc
; __device__ __forceinline__ int crow(int r, int hi) { return (r & 3) + 8 * (r >> 2) + 4 * hi; }
; template <class TIn, class TOut, int QS, int KS, int OS, bool BIAS, bool PREF = true>
; __device__ __forceinline__ void causal_swa_block(const BlockRef<TIn, TOut>& cur, const BlockRef<TIn, TOut>& nxt, int skv, int W, char* lds, Seam<TIn>& S) {
;     ...
;     for (int r = 0; r < 16; ++r) { const int orow = crow(r, hi);
; #pragma unroll
;         for (int d0 = 0; d0 < 4; ++d0) { const float v = o[d0][r] * rli[r];
;             if constexpr (same_t<TOut, float>::v) { Ow[(size_t)orow * OS + d0 * 32 + r32] = v; }
;             else { const float vn = __shfl_xor(v, 1);
;                    if ((r32 & 1) == 0) *(unsigned*)(Ow + (size_t)orow * OS + d0 * 32 + r32) = cvtpk(v, vn); } } }
; __device__ __forceinline__ void fox_phase(const Frame& F, char* lds, int& sg_first, int& sg_count) {
;     ...
;         { const int wt = Wwin / 64 + 4; int load[8], cnt[8];
; #pragma unroll
;           for (int i = 0; i < 8; ++i) { const int f0 = 4 * (i + 1), f1 = 4 * (16 - i); load[i] = (f0 < wt ? f0 : wt) + (f1 < wt ? f1 : wt); cnt[i] = 0; }
	global_store_dwordx2 v[70:71], v[42:43], off offset:64
	v_cndmask_b32_e64 v66, v26, v27, s[0:1]
	v_cndmask_b32_e64 v72, v28, v29, s[0:1]
	s_nop 0
	v_mov_b32_dpp v67, v66 quad_perm:[1,0,3,2] row_mask:0xf bank_mask:0xf
	v_mov_b32_dpp v73, v72 quad_perm:[1,0,3,2] row_mask:0xf bank_mask:0xf
	v_cndmask_b32_e64 v26, v67, v26, s[0:1]
	v_cndmask_b32_e64 v27, v27, v67, s[0:1]
	v_cndmask_b32_e64 v28, v73, v28, s[0:1]
	v_cndmask_b32_e64 v29, v29, v73, s[0:1]
	v_cvt_pk_bf16_f32 v26, v26, v27
	v_cvt_pk_bf16_f32 v28, v28, v29
	s_nop 0
	v_cndmask_b32_e32 v66, v26, v28, vcc
	s_nop 1
	v_mov_b32_dpp v67, v66 quad_perm:[2,3,0,1] row_mask:0xf bank_mask:0xf
	s_nop 0
	v_cndmask_b32_e32 v26, v67, v26, vcc
	v_cndmask_b32_e32 v27, v28, v67, vcc
	global_store_dwordx2 v[70:71], v[26:27], off offset:128
	v_cndmask_b32_e64 v66, v10, v11, s[0:1]
	v_cndmask_b32_e64 v72, v12, v13, s[0:1]
	s_nop 0
	v_mov_b32_dpp v67, v66 quad_perm:[1,0,3,2] row_mask:0xf bank_mask:0xf
	v_mov_b32_dpp v73, v72 quad_perm:[1,0,3,2] row_mask:0xf bank_mask:0xf
	v_cndmask_b32_e64 v10, v67, v10, s[0:1]
	v_cndmask_b32_e64 v11, v11, v67, s[0:1]
	v_cndmask_b32_e64 v12, v73, v12, s[0:1]
	v_cndmask_b32_e64 v13, v13, v73, s[0:1]
	v_cvt_pk_bf16_f32 v10, v10, v11
	v_cvt_pk_bf16_f32 v12, v12, v13
	s_nop 0
	v_cndmask_b32_e32 v66, v10, v12, vcc
	s_nop 1
	v_mov_b32_dpp v67, v66 quad_perm:[2,3,0,1] row_mask:0xf bank_mask:0xf
	s_nop 0
	v_cndmask_b32_e32 v10, v67, v10, vcc
	v_cndmask_b32_e32 v11, v12, v67, vcc
	global_store_dwordx2 v[70:71], v[10:11], off offset:192
	v_lshl_add_u64 v[70:71], v[70:71], 0, v[68:69]
	v_cndmask_b32_e64 v66, v62, v63, s[0:1]
	v_cndmask_b32_e64 v72, v64, v65, s[0:1]
	s_nop 0
	v_mov_b32_dpp v67, v66 quad_perm:[1,0,3,2] row_mask:0xf bank_mask:0xf
	v_mov_b32_dpp v73, v72 quad_perm:[1,0,3,2] row_mask:0xf bank_mask:0xf
	v_cndmask_b32_e64 v62, v67, v62, s[0:1]
	v_cndmask_b32_e64 v63, v63, v67, s[0:1]
	v_cndmask_b32_e64 v64, v73, v64, s[0:1]
	v_cndmask_b32_e64 v65, v65, v73, s[0:1]
	v_cvt_pk_bf16_f32 v62, v62, v63
	v_cvt_pk_bf16_f32 v64, v64, v65
	s_nop 0
	v_cndmask_b32_e32 v66, v62, v64, vcc
	s_nop 1
	v_mov_b32_dpp v67, v66 quad_perm:[2,3,0,1] row_mask:0xf bank_mask:0xf
	s_nop 0
	v_cndmask_b32_e32 v62, v67, v62, vcc
	v_cndmask_b32_e32 v63, v64, v67, vcc
	global_store_dwordx2 v[70:71], v[62:63], off
	v_cndmask_b32_e64 v66, v46, v47, s[0:1]
	v_cndmask_b32_e64 v72, v48, v49, s[0:1]
	s_nop 0
	v_mov_b32_dpp v67, v66 quad_perm:[1,0,3,2] row_mask:0xf bank_mask:0xf
	v_mov_b32_dpp v73, v72 quad_perm:[1,0,3,2] row_mask:0xf bank_mask:0xf
	v_cndmask_b32_e64 v46, v67, v46, s[0:1]
	v_cndmask_b32_e64 v47, v47, v67, s[0:1]
	v_cndmask_b32_e64 v48, v73, v48, s[0:1]
	v_cndmask_b32_e64 v49, v49, v73, s[0:1]
	v_cvt_pk_bf16_f32 v46, v46, v47
	v_cvt_pk_bf16_f32 v48, v48, v49
	s_nop 0
	v_cndmask_b32_e32 v66, v46, v48, vcc
	s_nop 1
	v_mov_b32_dpp v67, v66 quad_perm:[2,3,0,1] row_mask:0xf bank_mask:0xf
	s_nop 0
	v_cndmask_b32_e32 v46, v67, v46, vcc
	v_cndmask_b32_e32 v47, v48, v67, vcc
	global_store_dwordx2 v[70:71], v[46:47], off offset:64
	v_cndmask_b32_e64 v66, v30, v31, s[0:1]
	v_cndmask_b32_e64 v72, v32, v33, s[0:1]
	s_nop 0
	v_mov_b32_dpp v67, v66 quad_perm:[1,0,3,2] row_mask:0xf bank_mask:0xf
	v_mov_b32_dpp v73, v72 quad_perm:[1,0,3,2] row_mask:0xf bank_mask:0xf
	v_cndmask_b32_e64 v30, v67, v30, s[0:1]
	v_cndmask_b32_e64 v31, v31, v67, s[0:1]
	v_cndmask_b32_e64 v32, v73, v32, s[0:1]
	v_cndmask_b32_e64 v33, v33, v73, s[0:1]
	v_cvt_pk_bf16_f32 v30, v30, v31
	v_cvt_pk_bf16_f32 v32, v32, v33
	s_nop 0
	v_cndmask_b32_e32 v66, v30, v32, vcc
	s_nop 1
	v_mov_b32_dpp v67, v66 quad_perm:[2,3,0,1] row_mask:0xf bank_mask:0xf
	s_nop 0
	v_cndmask_b32_e32 v30, v67, v30, vcc
	v_cndmask_b32_e32 v31, v32, v67, vcc
	global_store_dwordx2 v[70:71], v[30:31], off offset:128
	v_cndmask_b32_e64 v66, v14, v15, s[0:1]
	v_cndmask_b32_e64 v72, v16, v17, s[0:1]
	s_nop 0
	v_mov_b32_dpp v67, v66 quad_perm:[1,0,3,2] row_mask:0xf bank_mask:0xf
	v_mov_b32_dpp v73, v72 quad_perm:[1,0,3,2] row_mask:0xf bank_mask:0xf
	v_cndmask_b32_e64 v14, v67, v14, s[0:1]
	v_cndmask_b32_e64 v15, v15, v67, s[0:1]
	v_cndmask_b32_e64 v16, v73, v16, s[0:1]
	v_cndmask_b32_e64 v17, v17, v73, s[0:1]
	v_cvt_pk_bf16_f32 v14, v14, v15
	v_cvt_pk_bf16_f32 v16, v16, v17
	s_nop 0
	v_cndmask_b32_e32 v66, v14, v16, vcc
	s_nop 1
	v_mov_b32_dpp v67, v66 quad_perm:[2,3,0,1] row_mask:0xf bank_mask:0xf
	s_nop 0
	v_cndmask_b32_e32 v14, v67, v14, vcc
	v_cndmask_b32_e32 v15, v16, v67, vcc
	global_store_dwordx2 v[70:71], v[14:15], off offset:192
	s_add_i32 s0, s9, 4
	v_and_b32_e32 v2, 7, v198
	v_lshlrev_b32_e32 v3, 2, v2
	v_add_u32_e32 v4, 4, v3
	v_sub_u32_e32 v5, 64, v3
	v_min_i32_e32 v4, s0, v4
	v_min_i32_e32 v5, s0, v5
	v_add_u32_e32 v4, v4, v5
	v_lshl_add_u32 v4, v4, 3, v2
	v_mov_b32_e32 v1, 0
	s_mov_b32 s7, 32
	s_waitcnt lgkmcnt(0)
	s_waitcnt vmcnt(63) expcnt(7) lgkmcnt(15)
	s_barrier
